# P6 SwiGLU epilogue re-emitted with packed f32 VALU ops (same per-element operation order), MFMA-drain nop blocks trimmed to one
# speedup vs baseline: 1.0327x; 1.0150x over previous
; __device__ __forceinline__ unsigned pk4_fp8(float a, float b, float c, float d) { int r = __builtin_amdgcn_cvt_pk_fp8_f32(a, b, 0, false); r = __builtin_amdgcn_cvt_pk_fp8_f32(c, d, r, true); return (unsigned)r; }
; template <class Epi, class Sched, bool ALIGN_EPI, bool FP8 = false>
; __device__ __forceinline__ void gemm_phase(PG8_LAS unsigned char* lds, const Gemm g, const Sched& S, const Epi& E, const int wid, const int lane) {
;     ...
;         if constexpr (FP8) {
; #pragma unroll
;             for (int a = 0; a < 2; ++a)
; #pragma unroll
;                 for (int b = 0; b < 2; ++b) asm volatile("s_nop 15\n\ts_nop 15" : "+v"(acc[a][b][0][0]), "+v"(acc[a][b][0][1]), "+v"(acc[a][b][1][0]), "+v"(acc[a][b][1][1]), "+v"(acc[a][b][2][0]), "+v"(acc[a][b][2][1]), "+v"(acc[a][b][3][0]), "+v"(acc[a][b][3][1]));
;         }
;     __device__ __forceinline__ void operator()(const f32x4 (&acc)[2][2][4][2], const Unit& u, int wr, int wc, int fr, int fq) const {
;         const int row0 = u.pm * BM + wr * 64 + fr, col0 = (u.pn & 3) * 128 + wc * 32 + 8 * fq;
; #pragma unroll
;         for (int ai = 0; ai < 2; ++ai)
; #pragma unroll
;             for (int m = 0; m < 4; ++m) { float r[8];
; #pragma unroll
;                 for (int n = 0; n < 2; ++n)
; #pragma unroll
;                     for (int e = 0; e < 4; ++e) { const float g = acc[ai][0][m][n][e], up = acc[ai][1][m][n][e]; r[4 * n + e] = g * __builtin_amdgcn_rcpf(1.0f + __builtin_amdgcn_exp2f(-g * LOG2E)) * up * (float)(1 << ASHIFT); }
;                 v2u w; w.x = pk4_fp8(r[0], r[1], r[2], r[3]); w.y = pk4_fp8(r[4], r[5], r[6], r[7]);
;                 *(v2u*)(O + (size_t)(row0 + ai * HALF + m * 16) * EH + col0) = w; }
;     }
.LBB0_751:
	s_mov_b32 s98, 0xbfb8aa3b
	s_mov_b32 s100, 0x41800000
	s_nop 15
	s_nop 15
	v_lshl_add_u32 v4, s88, 8, v203
	s_lshl_b32 s6, s89, 7
	s_and_b32 s6, s6, 0x180
	v_ashrrev_i32_e32 v5, 31, v4
	v_add_u32_e32 v2, s6, v205
	v_lshlrev_b64 v[0:1], 9, v[4:5]
	v_ashrrev_i32_e32 v3, 31, v2
	v_lshl_add_u64 v[0:1], s[24:25], 0, v[0:1]
	v_lshl_add_u64 v[0:1], v[0:1], 0, v[2:3]
	v_pk_mul_f32 v[228:229], v[192:193], s[98:99] op_sel_hi:[1,0]
	v_pk_mul_f32 v[230:231], v[194:195], s[98:99] op_sel_hi:[1,0]
	v_pk_mul_f32 v[232:233], v[184:185], s[98:99] op_sel_hi:[1,0]
	v_pk_mul_f32 v[234:235], v[186:187], s[98:99] op_sel_hi:[1,0]
	v_exp_f32_e32 v228, v228
	v_exp_f32_e32 v229, v229
	v_exp_f32_e32 v230, v230
	v_exp_f32_e32 v231, v231
	v_exp_f32_e32 v232, v232
	v_exp_f32_e32 v233, v233
	v_exp_f32_e32 v234, v234
	v_exp_f32_e32 v235, v235
	v_pk_add_f32 v[228:229], v[228:229], 1.0 op_sel_hi:[1,0]
	v_pk_add_f32 v[230:231], v[230:231], 1.0 op_sel_hi:[1,0]
	v_pk_add_f32 v[232:233], v[232:233], 1.0 op_sel_hi:[1,0]
	v_pk_add_f32 v[234:235], v[234:235], 1.0 op_sel_hi:[1,0]
	v_rcp_f32_e32 v228, v228
	v_rcp_f32_e32 v229, v229
	v_rcp_f32_e32 v230, v230
	v_rcp_f32_e32 v231, v231
	v_rcp_f32_e32 v232, v232
	v_rcp_f32_e32 v233, v233
	v_rcp_f32_e32 v234, v234
	v_rcp_f32_e32 v235, v235
	v_pk_mul_f32 v[228:229], v[192:193], v[228:229]
	v_pk_mul_f32 v[230:231], v[194:195], v[230:231]
	v_pk_mul_f32 v[232:233], v[184:185], v[232:233]
	v_pk_mul_f32 v[234:235], v[186:187], v[234:235]
	v_pk_mul_f32 v[228:229], v[188:189], v[228:229]
	v_pk_mul_f32 v[230:231], v[190:191], v[230:231]
	v_pk_mul_f32 v[232:233], v[180:181], v[232:233]
	v_pk_mul_f32 v[234:235], v[182:183], v[234:235]
	v_pk_mul_f32 v[228:229], s[100:101], v[228:229] op_sel_hi:[0,1]
	v_pk_mul_f32 v[230:231], s[100:101], v[230:231] op_sel_hi:[0,1]
	v_pk_mul_f32 v[232:233], s[100:101], v[232:233] op_sel_hi:[0,1]
	v_pk_mul_f32 v[234:235], s[100:101], v[234:235] op_sel_hi:[0,1]
	v_mov_b32_e32 v244, 0
	v_mov_b32_e32 v245, 0
	v_cvt_pk_fp8_f32 v244, v228, v229
	v_cvt_pk_fp8_f32 v245, v232, v233
	v_cvt_pk_fp8_f32 v244, v230, v231 op_sel:[0,0,1]
	v_cvt_pk_fp8_f32 v245, v234, v235 op_sel:[0,0,1]
	s_nop 0
	global_store_dwordx2 v[0:1], v[244:245], off
	v_or_b32_e32 v8, 16, v4
	v_ashrrev_i32_e32 v9, 31, v8
	v_lshlrev_b64 v[8:9], 9, v[8:9]
	v_lshl_add_u64 v[8:9], s[24:25], 0, v[8:9]
	v_lshl_add_u64 v[8:9], v[8:9], 0, v[2:3]
	v_pk_mul_f32 v[228:229], v[176:177], s[98:99] op_sel_hi:[1,0]
	v_pk_mul_f32 v[230:231], v[178:179], s[98:99] op_sel_hi:[1,0]
	v_pk_mul_f32 v[232:233], v[168:169], s[98:99] op_sel_hi:[1,0]
	v_pk_mul_f32 v[234:235], v[170:171], s[98:99] op_sel_hi:[1,0]
	v_exp_f32_e32 v228, v228
	v_exp_f32_e32 v229, v229
	v_exp_f32_e32 v230, v230
	v_exp_f32_e32 v231, v231
	v_exp_f32_e32 v232, v232
	v_exp_f32_e32 v233, v233
	v_exp_f32_e32 v234, v234
	v_exp_f32_e32 v235, v235
	v_pk_add_f32 v[228:229], v[228:229], 1.0 op_sel_hi:[1,0]
	v_pk_add_f32 v[230:231], v[230:231], 1.0 op_sel_hi:[1,0]
	v_pk_add_f32 v[232:233], v[232:233], 1.0 op_sel_hi:[1,0]
	v_pk_add_f32 v[234:235], v[234:235], 1.0 op_sel_hi:[1,0]
	v_rcp_f32_e32 v228, v228
	v_rcp_f32_e32 v229, v229
	v_rcp_f32_e32 v230, v230
	v_rcp_f32_e32 v231, v231
	v_rcp_f32_e32 v232, v232
	v_rcp_f32_e32 v233, v233
	v_rcp_f32_e32 v234, v234
	v_rcp_f32_e32 v235, v235
	v_pk_mul_f32 v[228:229], v[176:177], v[228:229]
	v_pk_mul_f32 v[230:231], v[178:179], v[230:231]
	v_pk_mul_f32 v[232:233], v[168:169], v[232:233]
	v_pk_mul_f32 v[234:235], v[170:171], v[234:235]
	v_pk_mul_f32 v[228:229], v[172:173], v[228:229]
	v_pk_mul_f32 v[230:231], v[174:175], v[230:231]
	v_pk_mul_f32 v[232:233], v[164:165], v[232:233]
	v_pk_mul_f32 v[234:235], v[166:167], v[234:235]
	v_pk_mul_f32 v[228:229], s[100:101], v[228:229] op_sel_hi:[0,1]
	v_pk_mul_f32 v[230:231], s[100:101], v[230:231] op_sel_hi:[0,1]
	v_pk_mul_f32 v[232:233], s[100:101], v[232:233] op_sel_hi:[0,1]
	v_pk_mul_f32 v[234:235], s[100:101], v[234:235] op_sel_hi:[0,1]
	v_mov_b32_e32 v244, 0
	v_mov_b32_e32 v245, 0
	v_cvt_pk_fp8_f32 v244, v228, v229
	v_cvt_pk_fp8_f32 v245, v232, v233
	v_cvt_pk_fp8_f32 v244, v230, v231 op_sel:[0,0,1]
	v_cvt_pk_fp8_f32 v245, v234, v235 op_sel:[0,0,1]
	s_nop 0
	global_store_dwordx2 v[8:9], v[244:245], off
	v_or_b32_e32 v8, 32, v4
	v_ashrrev_i32_e32 v9, 31, v8
	v_lshlrev_b64 v[8:9], 9, v[8:9]
	v_lshl_add_u64 v[8:9], s[24:25], 0, v[8:9]
	v_lshl_add_u64 v[8:9], v[8:9], 0, v[2:3]
	v_pk_mul_f32 v[228:229], v[160:161], s[98:99] op_sel_hi:[1,0]
	v_pk_mul_f32 v[230:231], v[162:163], s[98:99] op_sel_hi:[1,0]
	v_pk_mul_f32 v[232:233], v[152:153], s[98:99] op_sel_hi:[1,0]
	v_pk_mul_f32 v[234:235], v[154:155], s[98:99] op_sel_hi:[1,0]
	v_exp_f32_e32 v228, v228
	v_exp_f32_e32 v229, v229
	v_exp_f32_e32 v230, v230
	v_exp_f32_e32 v231, v231
	v_exp_f32_e32 v232, v232
	v_exp_f32_e32 v233, v233
	v_exp_f32_e32 v234, v234
	v_exp_f32_e32 v235, v235
	v_pk_add_f32 v[228:229], v[228:229], 1.0 op_sel_hi:[1,0]
	v_pk_add_f32 v[230:231], v[230:231], 1.0 op_sel_hi:[1,0]
	v_pk_add_f32 v[232:233], v[232:233], 1.0 op_sel_hi:[1,0]
	v_pk_add_f32 v[234:235], v[234:235], 1.0 op_sel_hi:[1,0]
	v_rcp_f32_e32 v228, v228
	v_rcp_f32_e32 v229, v229
	v_rcp_f32_e32 v230, v230
	v_rcp_f32_e32 v231, v231
	v_rcp_f32_e32 v232, v232
	v_rcp_f32_e32 v233, v233
	v_rcp_f32_e32 v234, v234
	v_rcp_f32_e32 v235, v235
	v_pk_mul_f32 v[228:229], v[160:161], v[228:229]
	v_pk_mul_f32 v[230:231], v[162:163], v[230:231]
	v_pk_mul_f32 v[232:233], v[152:153], v[232:233]
	v_pk_mul_f32 v[234:235], v[154:155], v[234:235]
	v_pk_mul_f32 v[228:229], v[156:157], v[228:229]
	v_pk_mul_f32 v[230:231], v[158:159], v[230:231]
	v_pk_mul_f32 v[232:233], v[148:149], v[232:233]
	v_pk_mul_f32 v[234:235], v[150:151], v[234:235]
; __device__ __forceinline__ unsigned pk4_fp8(float a, float b, float c, float d) { int r = __builtin_amdgcn_cvt_pk_fp8_f32(a, b, 0, false); r = __builtin_amdgcn_cvt_pk_fp8_f32(c, d, r, true); return (unsigned)r; }
;     __device__ __forceinline__ void operator()(const f32x4 (&acc)[2][2][4][2], const Unit& u, int wr, int wc, int fr, int fq) const {
;         const int row0 = u.pm * BM + wr * 64 + fr, col0 = (u.pn & 3) * 128 + wc * 32 + 8 * fq;
; #pragma unroll
;         for (int ai = 0; ai < 2; ++ai)
; #pragma unroll
;             for (int m = 0; m < 4; ++m) { float r[8];
; #pragma unroll
;                 for (int n = 0; n < 2; ++n)
; #pragma unroll
;                     for (int e = 0; e < 4; ++e) { const float g = acc[ai][0][m][n][e], up = acc[ai][1][m][n][e]; r[4 * n + e] = g * __builtin_amdgcn_rcpf(1.0f + __builtin_amdgcn_exp2f(-g * LOG2E)) * up * (float)(1 << ASHIFT); }
;                 v2u w; w.x = pk4_fp8(r[0], r[1], r[2], r[3]); w.y = pk4_fp8(r[4], r[5], r[6], r[7]);
;                 *(v2u*)(O + (size_t)(row0 + ai * HALF + m * 16) * EH + col0) = w; }
;     }
	v_pk_mul_f32 v[228:229], s[100:101], v[228:229] op_sel_hi:[0,1]
	v_pk_mul_f32 v[230:231], s[100:101], v[230:231] op_sel_hi:[0,1]
	v_pk_mul_f32 v[232:233], s[100:101], v[232:233] op_sel_hi:[0,1]
	v_pk_mul_f32 v[234:235], s[100:101], v[234:235] op_sel_hi:[0,1]
	v_mov_b32_e32 v244, 0
	v_mov_b32_e32 v245, 0
	v_cvt_pk_fp8_f32 v244, v228, v229
	v_cvt_pk_fp8_f32 v245, v232, v233
	v_cvt_pk_fp8_f32 v244, v230, v231 op_sel:[0,0,1]
	v_cvt_pk_fp8_f32 v245, v234, v235 op_sel:[0,0,1]
	s_nop 0
	global_store_dwordx2 v[8:9], v[244:245], off
	v_or_b32_e32 v4, 48, v4
	v_ashrrev_i32_e32 v5, 31, v4
	v_lshlrev_b64 v[4:5], 9, v[4:5]
	v_lshl_add_u64 v[4:5], s[24:25], 0, v[4:5]
	v_lshl_add_u64 v[2:3], v[4:5], 0, v[2:3]
	v_pk_mul_f32 v[228:229], v[144:145], s[98:99] op_sel_hi:[1,0]
	v_pk_mul_f32 v[230:231], v[146:147], s[98:99] op_sel_hi:[1,0]
	v_pk_mul_f32 v[232:233], v[136:137], s[98:99] op_sel_hi:[1,0]
	v_pk_mul_f32 v[234:235], v[138:139], s[98:99] op_sel_hi:[1,0]
	v_exp_f32_e32 v228, v228
	v_exp_f32_e32 v229, v229
	v_exp_f32_e32 v230, v230
	v_exp_f32_e32 v231, v231
	v_exp_f32_e32 v232, v232
	v_exp_f32_e32 v233, v233
	v_exp_f32_e32 v234, v234
	v_exp_f32_e32 v235, v235
	v_pk_add_f32 v[228:229], v[228:229], 1.0 op_sel_hi:[1,0]
	v_pk_add_f32 v[230:231], v[230:231], 1.0 op_sel_hi:[1,0]
	v_pk_add_f32 v[232:233], v[232:233], 1.0 op_sel_hi:[1,0]
	v_pk_add_f32 v[234:235], v[234:235], 1.0 op_sel_hi:[1,0]
	v_rcp_f32_e32 v228, v228
	v_rcp_f32_e32 v229, v229
	v_rcp_f32_e32 v230, v230
	v_rcp_f32_e32 v231, v231
	v_rcp_f32_e32 v232, v232
	v_rcp_f32_e32 v233, v233
	v_rcp_f32_e32 v234, v234
	v_rcp_f32_e32 v235, v235
	v_pk_mul_f32 v[228:229], v[144:145], v[228:229]
	v_pk_mul_f32 v[230:231], v[146:147], v[230:231]
	v_pk_mul_f32 v[232:233], v[136:137], v[232:233]
	v_pk_mul_f32 v[234:235], v[138:139], v[234:235]
	v_pk_mul_f32 v[228:229], v[140:141], v[228:229]
	v_pk_mul_f32 v[230:231], v[142:143], v[230:231]
	v_pk_mul_f32 v[232:233], v[132:133], v[232:233]
	v_pk_mul_f32 v[234:235], v[134:135], v[234:235]
	v_pk_mul_f32 v[228:229], s[100:101], v[228:229] op_sel_hi:[0,1]
	v_pk_mul_f32 v[230:231], s[100:101], v[230:231] op_sel_hi:[0,1]
	v_pk_mul_f32 v[232:233], s[100:101], v[232:233] op_sel_hi:[0,1]
	v_pk_mul_f32 v[234:235], s[100:101], v[234:235] op_sel_hi:[0,1]
	v_mov_b32_e32 v244, 0
	v_mov_b32_e32 v245, 0
	v_cvt_pk_fp8_f32 v244, v228, v229
	v_cvt_pk_fp8_f32 v245, v232, v233
	v_cvt_pk_fp8_f32 v244, v230, v231 op_sel:[0,0,1]
	v_cvt_pk_fp8_f32 v245, v234, v235 op_sel:[0,0,1]
	s_nop 0
	global_store_dwordx2 v[2:3], v[244:245], off
	v_add_co_u32_e32 v4, vcc, s50, v0
	s_nop 0
	v_addc_co_u32_e32 v5, vcc, 0, v1, vcc
	v_pk_mul_f32 v[228:229], v[128:129], s[98:99] op_sel_hi:[1,0]
	v_pk_mul_f32 v[230:231], v[130:131], s[98:99] op_sel_hi:[1,0]
	v_pk_mul_f32 v[232:233], v[120:121], s[98:99] op_sel_hi:[1,0]
	v_pk_mul_f32 v[234:235], v[122:123], s[98:99] op_sel_hi:[1,0]
	v_exp_f32_e32 v228, v228
	v_exp_f32_e32 v229, v229
	v_exp_f32_e32 v230, v230
	v_exp_f32_e32 v231, v231
	v_exp_f32_e32 v232, v232
	v_exp_f32_e32 v233, v233
	v_exp_f32_e32 v234, v234
	v_exp_f32_e32 v235, v235
	v_pk_add_f32 v[228:229], v[228:229], 1.0 op_sel_hi:[1,0]
	v_pk_add_f32 v[230:231], v[230:231], 1.0 op_sel_hi:[1,0]
	v_pk_add_f32 v[232:233], v[232:233], 1.0 op_sel_hi:[1,0]
	v_pk_add_f32 v[234:235], v[234:235], 1.0 op_sel_hi:[1,0]
	v_rcp_f32_e32 v228, v228
	v_rcp_f32_e32 v229, v229
	v_rcp_f32_e32 v230, v230
	v_rcp_f32_e32 v231, v231
	v_rcp_f32_e32 v232, v232
	v_rcp_f32_e32 v233, v233
	v_rcp_f32_e32 v234, v234
	v_rcp_f32_e32 v235, v235
	v_pk_mul_f32 v[228:229], v[128:129], v[228:229]
	v_pk_mul_f32 v[230:231], v[130:131], v[230:231]
	v_pk_mul_f32 v[232:233], v[120:121], v[232:233]
	v_pk_mul_f32 v[234:235], v[122:123], v[234:235]
	v_pk_mul_f32 v[228:229], v[124:125], v[228:229]
	v_pk_mul_f32 v[230:231], v[126:127], v[230:231]
	v_pk_mul_f32 v[232:233], v[116:117], v[232:233]
	v_pk_mul_f32 v[234:235], v[118:119], v[234:235]
	v_pk_mul_f32 v[228:229], s[100:101], v[228:229] op_sel_hi:[0,1]
	v_pk_mul_f32 v[230:231], s[100:101], v[230:231] op_sel_hi:[0,1]
	v_pk_mul_f32 v[232:233], s[100:101], v[232:233] op_sel_hi:[0,1]
	v_pk_mul_f32 v[234:235], s[100:101], v[234:235] op_sel_hi:[0,1]
	v_mov_b32_e32 v244, 0
	v_mov_b32_e32 v245, 0
	v_cvt_pk_fp8_f32 v244, v228, v229
	v_cvt_pk_fp8_f32 v245, v232, v233
	v_cvt_pk_fp8_f32 v244, v230, v231 op_sel:[0,0,1]
	v_cvt_pk_fp8_f32 v245, v234, v235 op_sel:[0,0,1]
	s_nop 0
	global_store_dwordx2 v[4:5], v[244:245], off
	v_add_co_u32_e32 v4, vcc, s52, v0
	s_nop 0
	v_addc_co_u32_e32 v5, vcc, 0, v1, vcc
	v_pk_mul_f32 v[228:229], v[112:113], s[98:99] op_sel_hi:[1,0]
	v_pk_mul_f32 v[230:231], v[114:115], s[98:99] op_sel_hi:[1,0]
	v_pk_mul_f32 v[232:233], v[104:105], s[98:99] op_sel_hi:[1,0]
	v_pk_mul_f32 v[234:235], v[106:107], s[98:99] op_sel_hi:[1,0]
	v_exp_f32_e32 v228, v228
	v_exp_f32_e32 v229, v229
	v_exp_f32_e32 v230, v230
	v_exp_f32_e32 v231, v231
	v_exp_f32_e32 v232, v232
	v_exp_f32_e32 v233, v233
	v_exp_f32_e32 v234, v234
	v_exp_f32_e32 v235, v235
	v_pk_add_f32 v[228:229], v[228:229], 1.0 op_sel_hi:[1,0]
	v_pk_add_f32 v[230:231], v[230:231], 1.0 op_sel_hi:[1,0]
	v_pk_add_f32 v[232:233], v[232:233], 1.0 op_sel_hi:[1,0]
; #define PG8_BAR __builtin_amdgcn_s_barrier()
; __device__ __forceinline__ unsigned pk4_fp8(float a, float b, float c, float d) { int r = __builtin_amdgcn_cvt_pk_fp8_f32(a, b, 0, false); r = __builtin_amdgcn_cvt_pk_fp8_f32(c, d, r, true); return (unsigned)r; }
; template <class Epi, class Sched, bool ALIGN_EPI, bool FP8 = false>
; __device__ __forceinline__ void gemm_phase(PG8_LAS unsigned char* lds, const Gemm g, const Sched& S, const Epi& E, const int wid, const int lane) {
;     ...
;         E(acc, cur, wr, wc, fr, fq);
;         if (!has_next) break;
; #pragma unroll
;         for (int a = 0; a < 2; ++a)
; #pragma unroll
;             for (int b = 0; b < 2; ++b)
; #pragma unroll
;                 for (int m = 0; m < 4; ++m)
; #pragma unroll
;                     for (int n = 0; n < 2; ++n) acc[a][b][m][n] = (f32x4){0.f, 0.f, 0.f, 0.f};
;         cur = nxt; cA = nA; cB = nB; ++ui;
;         if constexpr (ALIGN_EPI) { if (wr == 1) PG8_BAR; }
;     __device__ __forceinline__ void operator()(const f32x4 (&acc)[2][2][4][2], const Unit& u, int wr, int wc, int fr, int fq) const {
;         const int row0 = u.pm * BM + wr * 64 + fr, col0 = (u.pn & 3) * 128 + wc * 32 + 8 * fq;
; #pragma unroll
;         for (int ai = 0; ai < 2; ++ai)
; #pragma unroll
;             for (int m = 0; m < 4; ++m) { float r[8];
; #pragma unroll
;                 for (int n = 0; n < 2; ++n)
; #pragma unroll
;                     for (int e = 0; e < 4; ++e) { const float g = acc[ai][0][m][n][e], up = acc[ai][1][m][n][e]; r[4 * n + e] = g * __builtin_amdgcn_rcpf(1.0f + __builtin_amdgcn_exp2f(-g * LOG2E)) * up * (float)(1 << ASHIFT); }
;                 v2u w; w.x = pk4_fp8(r[0], r[1], r[2], r[3]); w.y = pk4_fp8(r[4], r[5], r[6], r[7]);
;                 *(v2u*)(O + (size_t)(row0 + ai * HALF + m * 16) * EH + col0) = w; }
;     }
	v_pk_add_f32 v[234:235], v[234:235], 1.0 op_sel_hi:[1,0]
	v_rcp_f32_e32 v228, v228
	v_rcp_f32_e32 v229, v229
	v_rcp_f32_e32 v230, v230
	v_rcp_f32_e32 v231, v231
	v_rcp_f32_e32 v232, v232
	v_rcp_f32_e32 v233, v233
	v_rcp_f32_e32 v234, v234
	v_rcp_f32_e32 v235, v235
	v_pk_mul_f32 v[228:229], v[112:113], v[228:229]
	v_pk_mul_f32 v[230:231], v[114:115], v[230:231]
	v_pk_mul_f32 v[232:233], v[104:105], v[232:233]
	v_pk_mul_f32 v[234:235], v[106:107], v[234:235]
	v_pk_mul_f32 v[228:229], v[108:109], v[228:229]
	v_pk_mul_f32 v[230:231], v[110:111], v[230:231]
	v_pk_mul_f32 v[232:233], v[100:101], v[232:233]
	v_pk_mul_f32 v[234:235], v[102:103], v[234:235]
	v_pk_mul_f32 v[228:229], s[100:101], v[228:229] op_sel_hi:[0,1]
	v_pk_mul_f32 v[230:231], s[100:101], v[230:231] op_sel_hi:[0,1]
	v_pk_mul_f32 v[232:233], s[100:101], v[232:233] op_sel_hi:[0,1]
	v_pk_mul_f32 v[234:235], s[100:101], v[234:235] op_sel_hi:[0,1]
	v_mov_b32_e32 v244, 0
	v_mov_b32_e32 v245, 0
	v_cvt_pk_fp8_f32 v244, v228, v229
	v_cvt_pk_fp8_f32 v245, v232, v233
	v_cvt_pk_fp8_f32 v244, v230, v231 op_sel:[0,0,1]
	v_cvt_pk_fp8_f32 v245, v234, v235 op_sel:[0,0,1]
	s_nop 0
	global_store_dwordx2 v[4:5], v[244:245], off
	v_add_co_u32_e32 v4, vcc, s54, v0
	s_nop 0
	v_addc_co_u32_e32 v5, vcc, 0, v1, vcc
	v_pk_mul_f32 v[228:229], v[96:97], s[98:99] op_sel_hi:[1,0]
	v_pk_mul_f32 v[230:231], v[98:99], s[98:99] op_sel_hi:[1,0]
	v_pk_mul_f32 v[232:233], v[88:89], s[98:99] op_sel_hi:[1,0]
	v_pk_mul_f32 v[234:235], v[90:91], s[98:99] op_sel_hi:[1,0]
	v_exp_f32_e32 v228, v228
	v_exp_f32_e32 v229, v229
	v_exp_f32_e32 v230, v230
	v_exp_f32_e32 v231, v231
	v_exp_f32_e32 v232, v232
	v_exp_f32_e32 v233, v233
	v_exp_f32_e32 v234, v234
	v_exp_f32_e32 v235, v235
	v_pk_add_f32 v[228:229], v[228:229], 1.0 op_sel_hi:[1,0]
	v_pk_add_f32 v[230:231], v[230:231], 1.0 op_sel_hi:[1,0]
	v_pk_add_f32 v[232:233], v[232:233], 1.0 op_sel_hi:[1,0]
	v_pk_add_f32 v[234:235], v[234:235], 1.0 op_sel_hi:[1,0]
	v_rcp_f32_e32 v228, v228
	v_rcp_f32_e32 v229, v229
	v_rcp_f32_e32 v230, v230
	v_rcp_f32_e32 v231, v231
	v_rcp_f32_e32 v232, v232
	v_rcp_f32_e32 v233, v233
	v_rcp_f32_e32 v234, v234
	v_rcp_f32_e32 v235, v235
	v_pk_mul_f32 v[228:229], v[96:97], v[228:229]
	v_pk_mul_f32 v[230:231], v[98:99], v[230:231]
	v_pk_mul_f32 v[232:233], v[88:89], v[232:233]
	v_pk_mul_f32 v[234:235], v[90:91], v[234:235]
	v_pk_mul_f32 v[228:229], v[92:93], v[228:229]
	v_pk_mul_f32 v[230:231], v[94:95], v[230:231]
	v_pk_mul_f32 v[232:233], v[84:85], v[232:233]
	v_pk_mul_f32 v[234:235], v[86:87], v[234:235]
	v_pk_mul_f32 v[228:229], s[100:101], v[228:229] op_sel_hi:[0,1]
	v_pk_mul_f32 v[230:231], s[100:101], v[230:231] op_sel_hi:[0,1]
	v_pk_mul_f32 v[232:233], s[100:101], v[232:233] op_sel_hi:[0,1]
	v_pk_mul_f32 v[234:235], s[100:101], v[234:235] op_sel_hi:[0,1]
	v_mov_b32_e32 v244, 0
	v_mov_b32_e32 v245, 0
	v_cvt_pk_fp8_f32 v244, v228, v229
	v_cvt_pk_fp8_f32 v245, v232, v233
	v_cvt_pk_fp8_f32 v244, v230, v231 op_sel:[0,0,1]
	v_cvt_pk_fp8_f32 v245, v234, v235 op_sel:[0,0,1]
	s_nop 0
	global_store_dwordx2 v[4:5], v[244:245], off
	v_add_co_u32_e32 v0, vcc, 0x16000, v0
	s_nop 1
	v_addc_co_u32_e32 v1, vcc, 0, v1, vcc
	s_and_b64 vcc, exec, s[4:5]
	s_mov_b64 s[4:5], -1
	v_pk_mul_f32 v[228:229], v[80:81], s[98:99] op_sel_hi:[1,0]
	v_pk_mul_f32 v[230:231], v[82:83], s[98:99] op_sel_hi:[1,0]
	v_pk_mul_f32 v[232:233], v[72:73], s[98:99] op_sel_hi:[1,0]
	v_pk_mul_f32 v[234:235], v[74:75], s[98:99] op_sel_hi:[1,0]
	v_exp_f32_e32 v228, v228
	v_exp_f32_e32 v229, v229
	v_exp_f32_e32 v230, v230
	v_exp_f32_e32 v231, v231
	v_exp_f32_e32 v232, v232
	v_exp_f32_e32 v233, v233
	v_exp_f32_e32 v234, v234
	v_exp_f32_e32 v235, v235
	v_pk_add_f32 v[228:229], v[228:229], 1.0 op_sel_hi:[1,0]
	v_pk_add_f32 v[230:231], v[230:231], 1.0 op_sel_hi:[1,0]
	v_pk_add_f32 v[232:233], v[232:233], 1.0 op_sel_hi:[1,0]
	v_pk_add_f32 v[234:235], v[234:235], 1.0 op_sel_hi:[1,0]
	v_rcp_f32_e32 v228, v228
	v_rcp_f32_e32 v229, v229
	v_rcp_f32_e32 v230, v230
	v_rcp_f32_e32 v231, v231
	v_rcp_f32_e32 v232, v232
	v_rcp_f32_e32 v233, v233
	v_rcp_f32_e32 v234, v234
	v_rcp_f32_e32 v235, v235
	v_pk_mul_f32 v[228:229], v[80:81], v[228:229]
	v_pk_mul_f32 v[230:231], v[82:83], v[230:231]
	v_pk_mul_f32 v[232:233], v[72:73], v[232:233]
	v_pk_mul_f32 v[234:235], v[74:75], v[234:235]
	v_pk_mul_f32 v[228:229], v[76:77], v[228:229]
	v_pk_mul_f32 v[230:231], v[78:79], v[230:231]
	v_pk_mul_f32 v[232:233], v[68:69], v[232:233]
	v_pk_mul_f32 v[234:235], v[70:71], v[234:235]
	v_pk_mul_f32 v[228:229], s[100:101], v[228:229] op_sel_hi:[0,1]
	v_pk_mul_f32 v[230:231], s[100:101], v[230:231] op_sel_hi:[0,1]
	v_pk_mul_f32 v[232:233], s[100:101], v[232:233] op_sel_hi:[0,1]
	v_pk_mul_f32 v[234:235], s[100:101], v[234:235] op_sel_hi:[0,1]
	v_mov_b32_e32 v244, 0
	v_mov_b32_e32 v245, 0
	v_cvt_pk_fp8_f32 v244, v228, v229
	v_cvt_pk_fp8_f32 v245, v232, v233
	v_cvt_pk_fp8_f32 v244, v230, v231 op_sel:[0,0,1]
	v_cvt_pk_fp8_f32 v245, v234, v235 op_sel:[0,0,1]
	s_nop 0
	global_store_dwordx2 v[0:1], v[244:245], off
	s_cbranch_vccnz .LBB0_715
	s_andn2_b64 vcc, exec, s[22:23]
	s_cbranch_vccnz .LBB0_714
	s_barrier
	s_branch .LBB0_714

; __device__ __forceinline__ unsigned pk4_fp8(float a, float b, float c, float d) { int r = __builtin_amdgcn_cvt_pk_fp8_f32(a, b, 0, false); r = __builtin_amdgcn_cvt_pk_fp8_f32(c, d, r, true); return (unsigned)r; }
; template <class Epi, class Sched, bool ALIGN_EPI, bool FP8 = false>
; __device__ __forceinline__ void gemm_phase(PG8_LAS unsigned char* lds, const Gemm g, const Sched& S, const Epi& E, const int wid, const int lane) {
;     ...
;         if constexpr (FP8) {
; #pragma unroll
;             for (int a = 0; a < 2; ++a)
; #pragma unroll
;                 for (int b = 0; b < 2; ++b) asm volatile("s_nop 15\n\ts_nop 15" : "+v"(acc[a][b][0][0]), "+v"(acc[a][b][0][1]), "+v"(acc[a][b][1][0]), "+v"(acc[a][b][1][1]), "+v"(acc[a][b][2][0]), "+v"(acc[a][b][2][1]), "+v"(acc[a][b][3][0]), "+v"(acc[a][b][3][1]));
;         }
;     __device__ __forceinline__ void operator()(const f32x4 (&acc)[2][2][4][2], const Unit& u, int wr, int wc, int fr, int fq) const {
;         const int row0 = u.pm * BM + wr * 64 + fr, col0 = (u.pn & 3) * 128 + wc * 32 + 8 * fq;
; #pragma unroll
;         for (int ai = 0; ai < 2; ++ai)
; #pragma unroll
;             for (int m = 0; m < 4; ++m) { float r[8];
; #pragma unroll
;                 for (int n = 0; n < 2; ++n)
; #pragma unroll
;                     for (int e = 0; e < 4; ++e) { const float g = acc[ai][0][m][n][e], up = acc[ai][1][m][n][e]; r[4 * n + e] = g * __builtin_amdgcn_rcpf(1.0f + __builtin_amdgcn_exp2f(-g * LOG2E)) * up * (float)(1 << ASHIFT); }
;                 v2u w; w.x = pk4_fp8(r[0], r[1], r[2], r[3]); w.y = pk4_fp8(r[4], r[5], r[6], r[7]);
;                 *(v2u*)(O + (size_t)(row0 + ai * HALF + m * 16) * EH + col0) = w; }
;     }
.LBB0_1661:
	s_mov_b32 s98, 0xbfb8aa3b
	s_mov_b32 s100, 0x41800000
	s_nop 15
	s_nop 15
	v_lshl_add_u32 v4, s87, 8, v203
	s_lshl_b32 s6, s88, 7
	s_and_b32 s6, s6, 0x180
	v_ashrrev_i32_e32 v5, 31, v4
	v_add_u32_e32 v2, s6, v205
	v_lshlrev_b64 v[0:1], 9, v[4:5]
	v_ashrrev_i32_e32 v3, 31, v2
	v_lshl_add_u64 v[0:1], s[24:25], 0, v[0:1]
	v_lshl_add_u64 v[0:1], v[0:1], 0, v[2:3]
	v_pk_mul_f32 v[228:229], v[192:193], s[98:99] op_sel_hi:[1,0]
	v_pk_mul_f32 v[230:231], v[194:195], s[98:99] op_sel_hi:[1,0]
	v_pk_mul_f32 v[232:233], v[184:185], s[98:99] op_sel_hi:[1,0]
	v_pk_mul_f32 v[234:235], v[186:187], s[98:99] op_sel_hi:[1,0]
	v_exp_f32_e32 v228, v228
	v_exp_f32_e32 v229, v229
	v_exp_f32_e32 v230, v230
	v_exp_f32_e32 v231, v231
	v_exp_f32_e32 v232, v232
	v_exp_f32_e32 v233, v233
	v_exp_f32_e32 v234, v234
	v_exp_f32_e32 v235, v235
	v_pk_add_f32 v[228:229], v[228:229], 1.0 op_sel_hi:[1,0]
	v_pk_add_f32 v[230:231], v[230:231], 1.0 op_sel_hi:[1,0]
	v_pk_add_f32 v[232:233], v[232:233], 1.0 op_sel_hi:[1,0]
	v_pk_add_f32 v[234:235], v[234:235], 1.0 op_sel_hi:[1,0]
	v_rcp_f32_e32 v228, v228
	v_rcp_f32_e32 v229, v229
	v_rcp_f32_e32 v230, v230
	v_rcp_f32_e32 v231, v231
	v_rcp_f32_e32 v232, v232
	v_rcp_f32_e32 v233, v233
	v_rcp_f32_e32 v234, v234
	v_rcp_f32_e32 v235, v235
	v_pk_mul_f32 v[228:229], v[192:193], v[228:229]
	v_pk_mul_f32 v[230:231], v[194:195], v[230:231]
	v_pk_mul_f32 v[232:233], v[184:185], v[232:233]
	v_pk_mul_f32 v[234:235], v[186:187], v[234:235]
	v_pk_mul_f32 v[228:229], v[188:189], v[228:229]
	v_pk_mul_f32 v[230:231], v[190:191], v[230:231]
	v_pk_mul_f32 v[232:233], v[180:181], v[232:233]
	v_pk_mul_f32 v[234:235], v[182:183], v[234:235]
	v_pk_mul_f32 v[228:229], s[100:101], v[228:229] op_sel_hi:[0,1]
	v_pk_mul_f32 v[230:231], s[100:101], v[230:231] op_sel_hi:[0,1]
	v_pk_mul_f32 v[232:233], s[100:101], v[232:233] op_sel_hi:[0,1]
	v_pk_mul_f32 v[234:235], s[100:101], v[234:235] op_sel_hi:[0,1]
	v_mov_b32_e32 v244, 0
	v_mov_b32_e32 v245, 0
	v_cvt_pk_fp8_f32 v244, v228, v229
	v_cvt_pk_fp8_f32 v245, v232, v233
	v_cvt_pk_fp8_f32 v244, v230, v231 op_sel:[0,0,1]
	v_cvt_pk_fp8_f32 v245, v234, v235 op_sel:[0,0,1]
	s_nop 0
	global_store_dwordx2 v[0:1], v[244:245], off
	v_or_b32_e32 v8, 16, v4
	v_ashrrev_i32_e32 v9, 31, v8
	v_lshlrev_b64 v[8:9], 9, v[8:9]
	v_lshl_add_u64 v[8:9], s[24:25], 0, v[8:9]
	v_lshl_add_u64 v[8:9], v[8:9], 0, v[2:3]
	v_pk_mul_f32 v[228:229], v[176:177], s[98:99] op_sel_hi:[1,0]
	v_pk_mul_f32 v[230:231], v[178:179], s[98:99] op_sel_hi:[1,0]
	v_pk_mul_f32 v[232:233], v[168:169], s[98:99] op_sel_hi:[1,0]
	v_pk_mul_f32 v[234:235], v[170:171], s[98:99] op_sel_hi:[1,0]
	v_exp_f32_e32 v228, v228
	v_exp_f32_e32 v229, v229
	v_exp_f32_e32 v230, v230
	v_exp_f32_e32 v231, v231
	v_exp_f32_e32 v232, v232
	v_exp_f32_e32 v233, v233
	v_exp_f32_e32 v234, v234
	v_exp_f32_e32 v235, v235
	v_pk_add_f32 v[228:229], v[228:229], 1.0 op_sel_hi:[1,0]
	v_pk_add_f32 v[230:231], v[230:231], 1.0 op_sel_hi:[1,0]
	v_pk_add_f32 v[232:233], v[232:233], 1.0 op_sel_hi:[1,0]
	v_pk_add_f32 v[234:235], v[234:235], 1.0 op_sel_hi:[1,0]
	v_rcp_f32_e32 v228, v228
	v_rcp_f32_e32 v229, v229
	v_rcp_f32_e32 v230, v230
	v_rcp_f32_e32 v231, v231
	v_rcp_f32_e32 v232, v232
	v_rcp_f32_e32 v233, v233
	v_rcp_f32_e32 v234, v234
	v_rcp_f32_e32 v235, v235
	v_pk_mul_f32 v[228:229], v[176:177], v[228:229]
	v_pk_mul_f32 v[230:231], v[178:179], v[230:231]
	v_pk_mul_f32 v[232:233], v[168:169], v[232:233]
	v_pk_mul_f32 v[234:235], v[170:171], v[234:235]
	v_pk_mul_f32 v[228:229], v[172:173], v[228:229]
	v_pk_mul_f32 v[230:231], v[174:175], v[230:231]
	v_pk_mul_f32 v[232:233], v[164:165], v[232:233]
	v_pk_mul_f32 v[234:235], v[166:167], v[234:235]
	v_pk_mul_f32 v[228:229], s[100:101], v[228:229] op_sel_hi:[0,1]
	v_pk_mul_f32 v[230:231], s[100:101], v[230:231] op_sel_hi:[0,1]
	v_pk_mul_f32 v[232:233], s[100:101], v[232:233] op_sel_hi:[0,1]
	v_pk_mul_f32 v[234:235], s[100:101], v[234:235] op_sel_hi:[0,1]
	v_mov_b32_e32 v244, 0
	v_mov_b32_e32 v245, 0
	v_cvt_pk_fp8_f32 v244, v228, v229
	v_cvt_pk_fp8_f32 v245, v232, v233
	v_cvt_pk_fp8_f32 v244, v230, v231 op_sel:[0,0,1]
	v_cvt_pk_fp8_f32 v245, v234, v235 op_sel:[0,0,1]
	s_nop 0
	global_store_dwordx2 v[8:9], v[244:245], off
	v_or_b32_e32 v8, 32, v4
	v_ashrrev_i32_e32 v9, 31, v8
	v_lshlrev_b64 v[8:9], 9, v[8:9]
	v_lshl_add_u64 v[8:9], s[24:25], 0, v[8:9]
	v_lshl_add_u64 v[8:9], v[8:9], 0, v[2:3]
	v_pk_mul_f32 v[228:229], v[160:161], s[98:99] op_sel_hi:[1,0]
	v_pk_mul_f32 v[230:231], v[162:163], s[98:99] op_sel_hi:[1,0]
	v_pk_mul_f32 v[232:233], v[152:153], s[98:99] op_sel_hi:[1,0]
	v_pk_mul_f32 v[234:235], v[154:155], s[98:99] op_sel_hi:[1,0]
	v_exp_f32_e32 v228, v228
	v_exp_f32_e32 v229, v229
	v_exp_f32_e32 v230, v230
	v_exp_f32_e32 v231, v231
	v_exp_f32_e32 v232, v232
	v_exp_f32_e32 v233, v233
	v_exp_f32_e32 v234, v234
	v_exp_f32_e32 v235, v235
	v_pk_add_f32 v[228:229], v[228:229], 1.0 op_sel_hi:[1,0]
	v_pk_add_f32 v[230:231], v[230:231], 1.0 op_sel_hi:[1,0]
	v_pk_add_f32 v[232:233], v[232:233], 1.0 op_sel_hi:[1,0]
	v_pk_add_f32 v[234:235], v[234:235], 1.0 op_sel_hi:[1,0]
	v_rcp_f32_e32 v228, v228
	v_rcp_f32_e32 v229, v229
	v_rcp_f32_e32 v230, v230
	v_rcp_f32_e32 v231, v231
	v_rcp_f32_e32 v232, v232
	v_rcp_f32_e32 v233, v233
	v_rcp_f32_e32 v234, v234
	v_rcp_f32_e32 v235, v235
	v_pk_mul_f32 v[228:229], v[160:161], v[228:229]
	v_pk_mul_f32 v[230:231], v[162:163], v[230:231]
	v_pk_mul_f32 v[232:233], v[152:153], v[232:233]
	v_pk_mul_f32 v[234:235], v[154:155], v[234:235]
	v_pk_mul_f32 v[228:229], v[156:157], v[228:229]
	v_pk_mul_f32 v[230:231], v[158:159], v[230:231]
	v_pk_mul_f32 v[232:233], v[148:149], v[232:233]
	v_pk_mul_f32 v[234:235], v[150:151], v[234:235]
; __device__ __forceinline__ unsigned pk4_fp8(float a, float b, float c, float d) { int r = __builtin_amdgcn_cvt_pk_fp8_f32(a, b, 0, false); r = __builtin_amdgcn_cvt_pk_fp8_f32(c, d, r, true); return (unsigned)r; }
;     __device__ __forceinline__ void operator()(const f32x4 (&acc)[2][2][4][2], const Unit& u, int wr, int wc, int fr, int fq) const {
;         const int row0 = u.pm * BM + wr * 64 + fr, col0 = (u.pn & 3) * 128 + wc * 32 + 8 * fq;
; #pragma unroll
;         for (int ai = 0; ai < 2; ++ai)
; #pragma unroll
;             for (int m = 0; m < 4; ++m) { float r[8];
; #pragma unroll
;                 for (int n = 0; n < 2; ++n)
; #pragma unroll
;                     for (int e = 0; e < 4; ++e) { const float g = acc[ai][0][m][n][e], up = acc[ai][1][m][n][e]; r[4 * n + e] = g * __builtin_amdgcn_rcpf(1.0f + __builtin_amdgcn_exp2f(-g * LOG2E)) * up * (float)(1 << ASHIFT); }
;                 v2u w; w.x = pk4_fp8(r[0], r[1], r[2], r[3]); w.y = pk4_fp8(r[4], r[5], r[6], r[7]);
;                 *(v2u*)(O + (size_t)(row0 + ai * HALF + m * 16) * EH + col0) = w; }
;     }
	v_pk_mul_f32 v[228:229], s[100:101], v[228:229] op_sel_hi:[0,1]
	v_pk_mul_f32 v[230:231], s[100:101], v[230:231] op_sel_hi:[0,1]
	v_pk_mul_f32 v[232:233], s[100:101], v[232:233] op_sel_hi:[0,1]
	v_pk_mul_f32 v[234:235], s[100:101], v[234:235] op_sel_hi:[0,1]
	v_mov_b32_e32 v244, 0
	v_mov_b32_e32 v245, 0
	v_cvt_pk_fp8_f32 v244, v228, v229
	v_cvt_pk_fp8_f32 v245, v232, v233
	v_cvt_pk_fp8_f32 v244, v230, v231 op_sel:[0,0,1]
	v_cvt_pk_fp8_f32 v245, v234, v235 op_sel:[0,0,1]
	s_nop 0
	global_store_dwordx2 v[8:9], v[244:245], off
	v_or_b32_e32 v4, 48, v4
	v_ashrrev_i32_e32 v5, 31, v4
	v_lshlrev_b64 v[4:5], 9, v[4:5]
	v_lshl_add_u64 v[4:5], s[24:25], 0, v[4:5]
	v_lshl_add_u64 v[2:3], v[4:5], 0, v[2:3]
	v_pk_mul_f32 v[228:229], v[144:145], s[98:99] op_sel_hi:[1,0]
	v_pk_mul_f32 v[230:231], v[146:147], s[98:99] op_sel_hi:[1,0]
	v_pk_mul_f32 v[232:233], v[136:137], s[98:99] op_sel_hi:[1,0]
	v_pk_mul_f32 v[234:235], v[138:139], s[98:99] op_sel_hi:[1,0]
	v_exp_f32_e32 v228, v228
	v_exp_f32_e32 v229, v229
	v_exp_f32_e32 v230, v230
	v_exp_f32_e32 v231, v231
	v_exp_f32_e32 v232, v232
	v_exp_f32_e32 v233, v233
	v_exp_f32_e32 v234, v234
	v_exp_f32_e32 v235, v235
	v_pk_add_f32 v[228:229], v[228:229], 1.0 op_sel_hi:[1,0]
	v_pk_add_f32 v[230:231], v[230:231], 1.0 op_sel_hi:[1,0]
	v_pk_add_f32 v[232:233], v[232:233], 1.0 op_sel_hi:[1,0]
	v_pk_add_f32 v[234:235], v[234:235], 1.0 op_sel_hi:[1,0]
	v_rcp_f32_e32 v228, v228
	v_rcp_f32_e32 v229, v229
	v_rcp_f32_e32 v230, v230
	v_rcp_f32_e32 v231, v231
	v_rcp_f32_e32 v232, v232
	v_rcp_f32_e32 v233, v233
	v_rcp_f32_e32 v234, v234
	v_rcp_f32_e32 v235, v235
	v_pk_mul_f32 v[228:229], v[144:145], v[228:229]
	v_pk_mul_f32 v[230:231], v[146:147], v[230:231]
	v_pk_mul_f32 v[232:233], v[136:137], v[232:233]
	v_pk_mul_f32 v[234:235], v[138:139], v[234:235]
	v_pk_mul_f32 v[228:229], v[140:141], v[228:229]
	v_pk_mul_f32 v[230:231], v[142:143], v[230:231]
	v_pk_mul_f32 v[232:233], v[132:133], v[232:233]
	v_pk_mul_f32 v[234:235], v[134:135], v[234:235]
	v_pk_mul_f32 v[228:229], s[100:101], v[228:229] op_sel_hi:[0,1]
	v_pk_mul_f32 v[230:231], s[100:101], v[230:231] op_sel_hi:[0,1]
	v_pk_mul_f32 v[232:233], s[100:101], v[232:233] op_sel_hi:[0,1]
	v_pk_mul_f32 v[234:235], s[100:101], v[234:235] op_sel_hi:[0,1]
	v_mov_b32_e32 v244, 0
	v_mov_b32_e32 v245, 0
	v_cvt_pk_fp8_f32 v244, v228, v229
	v_cvt_pk_fp8_f32 v245, v232, v233
	v_cvt_pk_fp8_f32 v244, v230, v231 op_sel:[0,0,1]
	v_cvt_pk_fp8_f32 v245, v234, v235 op_sel:[0,0,1]
	s_nop 0
	global_store_dwordx2 v[2:3], v[244:245], off
	v_add_co_u32_e32 v4, vcc, s50, v0
	s_nop 0
	v_addc_co_u32_e32 v5, vcc, 0, v1, vcc
	v_pk_mul_f32 v[228:229], v[128:129], s[98:99] op_sel_hi:[1,0]
	v_pk_mul_f32 v[230:231], v[130:131], s[98:99] op_sel_hi:[1,0]
	v_pk_mul_f32 v[232:233], v[120:121], s[98:99] op_sel_hi:[1,0]
	v_pk_mul_f32 v[234:235], v[122:123], s[98:99] op_sel_hi:[1,0]
	v_exp_f32_e32 v228, v228
	v_exp_f32_e32 v229, v229
	v_exp_f32_e32 v230, v230
	v_exp_f32_e32 v231, v231
	v_exp_f32_e32 v232, v232
	v_exp_f32_e32 v233, v233
	v_exp_f32_e32 v234, v234
	v_exp_f32_e32 v235, v235
	v_pk_add_f32 v[228:229], v[228:229], 1.0 op_sel_hi:[1,0]
	v_pk_add_f32 v[230:231], v[230:231], 1.0 op_sel_hi:[1,0]
	v_pk_add_f32 v[232:233], v[232:233], 1.0 op_sel_hi:[1,0]
	v_pk_add_f32 v[234:235], v[234:235], 1.0 op_sel_hi:[1,0]
	v_rcp_f32_e32 v228, v228
	v_rcp_f32_e32 v229, v229
	v_rcp_f32_e32 v230, v230
	v_rcp_f32_e32 v231, v231
	v_rcp_f32_e32 v232, v232
	v_rcp_f32_e32 v233, v233
	v_rcp_f32_e32 v234, v234
	v_rcp_f32_e32 v235, v235
	v_pk_mul_f32 v[228:229], v[128:129], v[228:229]
	v_pk_mul_f32 v[230:231], v[130:131], v[230:231]
	v_pk_mul_f32 v[232:233], v[120:121], v[232:233]
	v_pk_mul_f32 v[234:235], v[122:123], v[234:235]
	v_pk_mul_f32 v[228:229], v[124:125], v[228:229]
	v_pk_mul_f32 v[230:231], v[126:127], v[230:231]
	v_pk_mul_f32 v[232:233], v[116:117], v[232:233]
	v_pk_mul_f32 v[234:235], v[118:119], v[234:235]
	v_pk_mul_f32 v[228:229], s[100:101], v[228:229] op_sel_hi:[0,1]
	v_pk_mul_f32 v[230:231], s[100:101], v[230:231] op_sel_hi:[0,1]
	v_pk_mul_f32 v[232:233], s[100:101], v[232:233] op_sel_hi:[0,1]
	v_pk_mul_f32 v[234:235], s[100:101], v[234:235] op_sel_hi:[0,1]
	v_mov_b32_e32 v244, 0
	v_mov_b32_e32 v245, 0
	v_cvt_pk_fp8_f32 v244, v228, v229
	v_cvt_pk_fp8_f32 v245, v232, v233
	v_cvt_pk_fp8_f32 v244, v230, v231 op_sel:[0,0,1]
	v_cvt_pk_fp8_f32 v245, v234, v235 op_sel:[0,0,1]
	s_nop 0
	global_store_dwordx2 v[4:5], v[244:245], off
	v_add_co_u32_e32 v4, vcc, s52, v0
	s_nop 0
	v_addc_co_u32_e32 v5, vcc, 0, v1, vcc
	v_pk_mul_f32 v[228:229], v[112:113], s[98:99] op_sel_hi:[1,0]
	v_pk_mul_f32 v[230:231], v[114:115], s[98:99] op_sel_hi:[1,0]
	v_pk_mul_f32 v[232:233], v[104:105], s[98:99] op_sel_hi:[1,0]
	v_pk_mul_f32 v[234:235], v[106:107], s[98:99] op_sel_hi:[1,0]
	v_exp_f32_e32 v228, v228
	v_exp_f32_e32 v229, v229
	v_exp_f32_e32 v230, v230
	v_exp_f32_e32 v231, v231
	v_exp_f32_e32 v232, v232
	v_exp_f32_e32 v233, v233
	v_exp_f32_e32 v234, v234
	v_exp_f32_e32 v235, v235
	v_pk_add_f32 v[228:229], v[228:229], 1.0 op_sel_hi:[1,0]
	v_pk_add_f32 v[230:231], v[230:231], 1.0 op_sel_hi:[1,0]
	v_pk_add_f32 v[232:233], v[232:233], 1.0 op_sel_hi:[1,0]
; #define PG8_BAR __builtin_amdgcn_s_barrier()
; __device__ __forceinline__ unsigned pk4_fp8(float a, float b, float c, float d) { int r = __builtin_amdgcn_cvt_pk_fp8_f32(a, b, 0, false); r = __builtin_amdgcn_cvt_pk_fp8_f32(c, d, r, true); return (unsigned)r; }
; template <class Epi, class Sched, bool ALIGN_EPI, bool FP8 = false>
; __device__ __forceinline__ void gemm_phase(PG8_LAS unsigned char* lds, const Gemm g, const Sched& S, const Epi& E, const int wid, const int lane) {
;     ...
;         E(acc, cur, wr, wc, fr, fq);
;         if (!has_next) break;
; #pragma unroll
;         for (int a = 0; a < 2; ++a)
; #pragma unroll
;             for (int b = 0; b < 2; ++b)
; #pragma unroll
;                 for (int m = 0; m < 4; ++m)
; #pragma unroll
;                     for (int n = 0; n < 2; ++n) acc[a][b][m][n] = (f32x4){0.f, 0.f, 0.f, 0.f};
;         cur = nxt; cA = nA; cB = nB; ++ui;
;         if constexpr (ALIGN_EPI) { if (wr == 1) PG8_BAR; }
;     __device__ __forceinline__ void operator()(const f32x4 (&acc)[2][2][4][2], const Unit& u, int wr, int wc, int fr, int fq) const {
;         const int row0 = u.pm * BM + wr * 64 + fr, col0 = (u.pn & 3) * 128 + wc * 32 + 8 * fq;
; #pragma unroll
;         for (int ai = 0; ai < 2; ++ai)
; #pragma unroll
;             for (int m = 0; m < 4; ++m) { float r[8];
; #pragma unroll
;                 for (int n = 0; n < 2; ++n)
; #pragma unroll
;                     for (int e = 0; e < 4; ++e) { const float g = acc[ai][0][m][n][e], up = acc[ai][1][m][n][e]; r[4 * n + e] = g * __builtin_amdgcn_rcpf(1.0f + __builtin_amdgcn_exp2f(-g * LOG2E)) * up * (float)(1 << ASHIFT); }
;                 v2u w; w.x = pk4_fp8(r[0], r[1], r[2], r[3]); w.y = pk4_fp8(r[4], r[5], r[6], r[7]);
;                 *(v2u*)(O + (size_t)(row0 + ai * HALF + m * 16) * EH + col0) = w; }
;     }
	v_pk_add_f32 v[234:235], v[234:235], 1.0 op_sel_hi:[1,0]
	v_rcp_f32_e32 v228, v228
	v_rcp_f32_e32 v229, v229
	v_rcp_f32_e32 v230, v230
	v_rcp_f32_e32 v231, v231
	v_rcp_f32_e32 v232, v232
	v_rcp_f32_e32 v233, v233
	v_rcp_f32_e32 v234, v234
	v_rcp_f32_e32 v235, v235
	v_pk_mul_f32 v[228:229], v[112:113], v[228:229]
	v_pk_mul_f32 v[230:231], v[114:115], v[230:231]
	v_pk_mul_f32 v[232:233], v[104:105], v[232:233]
	v_pk_mul_f32 v[234:235], v[106:107], v[234:235]
	v_pk_mul_f32 v[228:229], v[108:109], v[228:229]
	v_pk_mul_f32 v[230:231], v[110:111], v[230:231]
	v_pk_mul_f32 v[232:233], v[100:101], v[232:233]
	v_pk_mul_f32 v[234:235], v[102:103], v[234:235]
	v_pk_mul_f32 v[228:229], s[100:101], v[228:229] op_sel_hi:[0,1]
	v_pk_mul_f32 v[230:231], s[100:101], v[230:231] op_sel_hi:[0,1]
	v_pk_mul_f32 v[232:233], s[100:101], v[232:233] op_sel_hi:[0,1]
	v_pk_mul_f32 v[234:235], s[100:101], v[234:235] op_sel_hi:[0,1]
	v_mov_b32_e32 v244, 0
	v_mov_b32_e32 v245, 0
	v_cvt_pk_fp8_f32 v244, v228, v229
	v_cvt_pk_fp8_f32 v245, v232, v233
	v_cvt_pk_fp8_f32 v244, v230, v231 op_sel:[0,0,1]
	v_cvt_pk_fp8_f32 v245, v234, v235 op_sel:[0,0,1]
	s_nop 0
	global_store_dwordx2 v[4:5], v[244:245], off
	v_add_co_u32_e32 v4, vcc, s54, v0
	s_nop 0
	v_addc_co_u32_e32 v5, vcc, 0, v1, vcc
	v_pk_mul_f32 v[228:229], v[96:97], s[98:99] op_sel_hi:[1,0]
	v_pk_mul_f32 v[230:231], v[98:99], s[98:99] op_sel_hi:[1,0]
	v_pk_mul_f32 v[232:233], v[88:89], s[98:99] op_sel_hi:[1,0]
	v_pk_mul_f32 v[234:235], v[90:91], s[98:99] op_sel_hi:[1,0]
	v_exp_f32_e32 v228, v228
	v_exp_f32_e32 v229, v229
	v_exp_f32_e32 v230, v230
	v_exp_f32_e32 v231, v231
	v_exp_f32_e32 v232, v232
	v_exp_f32_e32 v233, v233
	v_exp_f32_e32 v234, v234
	v_exp_f32_e32 v235, v235
	v_pk_add_f32 v[228:229], v[228:229], 1.0 op_sel_hi:[1,0]
	v_pk_add_f32 v[230:231], v[230:231], 1.0 op_sel_hi:[1,0]
	v_pk_add_f32 v[232:233], v[232:233], 1.0 op_sel_hi:[1,0]
	v_pk_add_f32 v[234:235], v[234:235], 1.0 op_sel_hi:[1,0]
	v_rcp_f32_e32 v228, v228
	v_rcp_f32_e32 v229, v229
	v_rcp_f32_e32 v230, v230
	v_rcp_f32_e32 v231, v231
	v_rcp_f32_e32 v232, v232
	v_rcp_f32_e32 v233, v233
	v_rcp_f32_e32 v234, v234
	v_rcp_f32_e32 v235, v235
	v_pk_mul_f32 v[228:229], v[96:97], v[228:229]
	v_pk_mul_f32 v[230:231], v[98:99], v[230:231]
	v_pk_mul_f32 v[232:233], v[88:89], v[232:233]
	v_pk_mul_f32 v[234:235], v[90:91], v[234:235]
	v_pk_mul_f32 v[228:229], v[92:93], v[228:229]
	v_pk_mul_f32 v[230:231], v[94:95], v[230:231]
	v_pk_mul_f32 v[232:233], v[84:85], v[232:233]
	v_pk_mul_f32 v[234:235], v[86:87], v[234:235]
	v_pk_mul_f32 v[228:229], s[100:101], v[228:229] op_sel_hi:[0,1]
	v_pk_mul_f32 v[230:231], s[100:101], v[230:231] op_sel_hi:[0,1]
	v_pk_mul_f32 v[232:233], s[100:101], v[232:233] op_sel_hi:[0,1]
	v_pk_mul_f32 v[234:235], s[100:101], v[234:235] op_sel_hi:[0,1]
	v_mov_b32_e32 v244, 0
	v_mov_b32_e32 v245, 0
	v_cvt_pk_fp8_f32 v244, v228, v229
	v_cvt_pk_fp8_f32 v245, v232, v233
	v_cvt_pk_fp8_f32 v244, v230, v231 op_sel:[0,0,1]
	v_cvt_pk_fp8_f32 v245, v234, v235 op_sel:[0,0,1]
	s_nop 0
	global_store_dwordx2 v[4:5], v[244:245], off
	v_add_co_u32_e32 v0, vcc, 0x16000, v0
	s_nop 1
	v_addc_co_u32_e32 v1, vcc, 0, v1, vcc
	s_and_b64 vcc, exec, s[4:5]
	s_mov_b64 s[4:5], -1
	v_pk_mul_f32 v[228:229], v[80:81], s[98:99] op_sel_hi:[1,0]
	v_pk_mul_f32 v[230:231], v[82:83], s[98:99] op_sel_hi:[1,0]
	v_pk_mul_f32 v[232:233], v[72:73], s[98:99] op_sel_hi:[1,0]
	v_pk_mul_f32 v[234:235], v[74:75], s[98:99] op_sel_hi:[1,0]
	v_exp_f32_e32 v228, v228
	v_exp_f32_e32 v229, v229
	v_exp_f32_e32 v230, v230
	v_exp_f32_e32 v231, v231
	v_exp_f32_e32 v232, v232
	v_exp_f32_e32 v233, v233
	v_exp_f32_e32 v234, v234
	v_exp_f32_e32 v235, v235
	v_pk_add_f32 v[228:229], v[228:229], 1.0 op_sel_hi:[1,0]
	v_pk_add_f32 v[230:231], v[230:231], 1.0 op_sel_hi:[1,0]
	v_pk_add_f32 v[232:233], v[232:233], 1.0 op_sel_hi:[1,0]
	v_pk_add_f32 v[234:235], v[234:235], 1.0 op_sel_hi:[1,0]
	v_rcp_f32_e32 v228, v228
	v_rcp_f32_e32 v229, v229
	v_rcp_f32_e32 v230, v230
	v_rcp_f32_e32 v231, v231
	v_rcp_f32_e32 v232, v232
	v_rcp_f32_e32 v233, v233
	v_rcp_f32_e32 v234, v234
	v_rcp_f32_e32 v235, v235
	v_pk_mul_f32 v[228:229], v[80:81], v[228:229]
	v_pk_mul_f32 v[230:231], v[82:83], v[230:231]
	v_pk_mul_f32 v[232:233], v[72:73], v[232:233]
	v_pk_mul_f32 v[234:235], v[74:75], v[234:235]
	v_pk_mul_f32 v[228:229], v[76:77], v[228:229]
	v_pk_mul_f32 v[230:231], v[78:79], v[230:231]
	v_pk_mul_f32 v[232:233], v[68:69], v[232:233]
	v_pk_mul_f32 v[234:235], v[70:71], v[234:235]
	v_pk_mul_f32 v[228:229], s[100:101], v[228:229] op_sel_hi:[0,1]
	v_pk_mul_f32 v[230:231], s[100:101], v[230:231] op_sel_hi:[0,1]
	v_pk_mul_f32 v[232:233], s[100:101], v[232:233] op_sel_hi:[0,1]
	v_pk_mul_f32 v[234:235], s[100:101], v[234:235] op_sel_hi:[0,1]
	v_mov_b32_e32 v244, 0
	v_mov_b32_e32 v245, 0
	v_cvt_pk_fp8_f32 v244, v228, v229
	v_cvt_pk_fp8_f32 v245, v232, v233
	v_cvt_pk_fp8_f32 v244, v230, v231 op_sel:[0,0,1]
	v_cvt_pk_fp8_f32 v245, v234, v235 op_sel:[0,0,1]
	s_nop 0
	global_store_dwordx2 v[0:1], v[244:245], off
	s_cbranch_vccnz .LBB0_1625
	s_andn2_b64 vcc, exec, s[22:23]
	s_cbranch_vccnz .LBB0_1624
	s_barrier
	s_branch .LBB0_1624
